# FFT phase converts 56 steps (was 64); layer-0 gate/up GEMM site now 1 piece every K iteration (16 steps)
# baseline (speedup 1.0000x reference)
;     __device__ __forceinline__ const char* a_base() const { return (const char*)A; }
; template <class Epi, class Sched>
; __device__ __forceinline__ void gemm_phase(LAS unsigned char* lds, const int K, const Sched& S, const Epi& E) {
;     const int tid = tid_fresh(), wid = __builtin_amdgcn_readfirstlane(tid >> 6), lane = tid & 63, wr = wid >> 2, wc = wid & 3, fr = lane & 15, fq = lane >> 4;
;     const int nt = K / BK;
;     int R0, C0, R1, C1; stage_rc(tid * 16, R0, C0); stage_rc(tid * 16 + 8192, R1, C1);
;     const int Rb0 = Epi::PERM ? ((R0 & ~31) + perm32(R0 & 31)) : R0, Rb1 = Epi::PERM ? ((R1 & ~31) + perm32(R1 & 31)) : R1;
;     const unsigned voffB0 = S.b_off(Rb0, C0), voffB1 = S.b_off(Rb1, C1);
;     const size_t kstep = (size_t)(BK * 2);
;     const size_t kstepB = S.b_kstep(), hstep = S.b_hstep();
;     const unsigned ldsw = (unsigned)wid * 1024u;
;     const int aoff = lds_byte(wr * 64 + fr, fq * 8), boff = lds_byte(wc * 32 + fr, fq * 8);
;     ...
;     Unit cur, nxt; int ui = 0;
;     if (!S.next(0, cur)) return;
;     f32x4 acc[2][2][4][2];
; #pragma unroll
;     for (int a = 0; a < 2; ++a)
; #pragma unroll
;         for (int b = 0; b < 2; ++b)
; #pragma unroll
;             for (int m = 0; m < 4; ++m)
; #pragma unroll
;                 for (int n = 0; n < 2; ++n) acc[a][b][m][n] = (f32x4){0.f, 0.f, 0.f, 0.f};
;     bf16x8 At[4][2], B0[2][2], B1[2][2];
;     const char* const gA = S.a_base();
;     unsigned c00, c01, c10, c11, n00, n01, n10, n11;
;     PG8_AOFFS(cur, c00, c01, c10, c11);
;     const char* cB = S.b_ptr(cur);
;     PG8_STAGE(PG8_SB(0, 0), cB, voffB0, voffB1); PG8_STAGE(PG8_SA(0, 0), gA, c00, c01); PG8_STAGE(PG8_SB(0, 1), cB + hstep, voffB0, voffB1); PG8_STAGE(PG8_SA(0, 1), gA, c10, c11);
;     __device__ __forceinline__ void a_off4(const Unit& u, int r0, int r1, unsigned& o00, unsigned& o01, unsigned& o10, unsigned& o11) const {
;         const int p0 = u.pm * BM + r0, p1 = u.pm * BM + r1, p2 = p0 + HALF, p3 = p1 + HALF;
;         if (u.e >= NE) { o00 = (unsigned)p0 * (unsigned)(D * 2); o01 = (unsigned)p1 * (unsigned)(D * 2); o10 = (unsigned)p2 * (unsigned)(D * 2); o11 = (unsigned)p3 * (unsigned)(D * 2); return; }
;         const int* lp = list + u.e * T;
;         int v0 = lp[p0], v1 = lp[p1], v2 = lp[p2], v3 = lp[p3];
;         asm volatile("" : "+v"(v0), "+v"(v1), "+v"(v2), "+v"(v3));
;         const int c = cnt[u.e];
.LBB0_1077:
	s_or_b64 exec, exec, s[0:1]
	v_readlane_b32 s2, v254, 5
	v_readlane_b32 s0, v254, 0
	s_and_b32 s3, s2, 3
	v_readlane_b32 s1, v254, 1
	s_lshl_b32 s29, s28, 2
	v_writelane_b32 v254, s3, 27
	s_lshl_b32 s3, s3, 12
	v_mov_b32_e32 v6, v0
	s_waitcnt lgkmcnt(0)
	s_barrier
	v_readlane_b32 s84, v254, 0
	v_readlane_b32 s85, v254, 1
	s_nop 1
	s_load_dwordx2 s[74:75], s[84:85], 0xd8
	s_load_dwordx2 s[76:77], s[84:85], 0xe0
	s_load_dwordx2 s[78:79], s[84:85], 0x118
	v_and_b32_e32 v252, 63, v0
	v_lshrrev_b32_e32 v253, 6, v0
	v_lshlrev_b32_e32 v238, 2, v252
	v_lshlrev_b32_e32 v252, 4, v252
	v_add_u32_e32 v239, 0x800, v238
	v_add_u32_e32 v240, 0x1000, v238
	v_add_u32_e32 v241, 0x1800, v238
	v_readlane_b32 s86, v254, 4
	v_readlane_b32 s87, v255, 40
	v_readfirstlane_b32 s88, v253
	s_nop 3
	s_lshl_b32 s71, s86, 3
	s_lshl_b32 s87, s87, 3
	s_add_u32 s87, s87, s88
	s_add_u32 s70, s87, 0x1c000
	s_mov_b32 s80, 0
	s_mov_b32 s82, 0
	s_mov_b32 s90, 0
	s_waitcnt lgkmcnt(0)
	v_writelane_b32 v255, s3, 24
	s_cmp_lt_i32 s2, s29
	s_nop 0
	v_readfirstlane_b32 s30, v6
	s_cbranch_scc0 .LBB0_1099
	v_ashrrev_i32_e32 v1, 31, v6
	v_lshrrev_b32_e32 v1, 26, v1
	v_add_u32_e32 v1, v6, v1
	v_ashrrev_i32_e32 v9, 6, v1
	v_bfe_i32 v1, v6, 27, 1
	v_lshlrev_b32_e32 v2, 4, v6
	v_lshrrev_b32_e32 v1, 22, v1
	v_add_u32_e32 v1, v2, v1
	v_and_b32_e32 v1, 0xfffffc00, v1
	v_sub_u32_e32 v1, v2, v1
	v_lshrrev_b32_e32 v3, 4, v1
	v_bitop3_b32 v10, v3, v1, 32 bitop3:0x6c
	v_ashrrev_i32_e32 v1, 31, v1
	v_lshrrev_b32_e32 v1, 26, v1
	s_load_dwordx2 s[0:1], s[0:1], 0x118
	v_lshlrev_b32_e32 v3, 3, v9
	v_add_u32_e32 v1, v10, v1
	v_and_b32_e32 v3, -16, v3
	v_ashrrev_i32_e32 v8, 6, v1
	v_add_u32_e32 v2, 0x2000, v2
	v_add_u32_e32 v1, v8, v3
	v_ashrrev_i32_e32 v3, 31, v2
	v_lshrrev_b32_e32 v3, 22, v3
	v_add_u32_e32 v3, v2, v3
	s_waitcnt lgkmcnt(0)
	s_add_u32 s31, s0, 0x3ec30000
	v_ashrrev_i32_e32 v11, 10, v3
	v_readlane_b32 s3, v254, 5
	s_addc_u32 s33, s1, 0
	v_mul_i32_i24_e32 v3, 0x400, v11
	s_and_b32 s2, s3, -4
	v_sub_u32_e32 v2, v2, v3
	s_add_i32 s2, s2, 0
	v_lshrrev_b32_e32 v3, 4, v2
	s_add_i32 s2, s2, 0x21160
	v_bitop3_b32 v12, v3, v2, 32 bitop3:0x6c
	v_mov_b32_e32 v3, s2
	ds_read_b32 v3, v3
	v_ashrrev_i32_e32 v4, 31, v12
	v_lshrrev_b32_e32 v4, 26, v4
	v_lshlrev_b32_e32 v2, 3, v11
	v_add_u32_e32 v4, v12, v4
	s_waitcnt lgkmcnt(0)
	v_lshlrev_b32_e32 v5, 2, v3
	v_add_u32_e32 v5, 0, v5
	v_add_u32_e32 v5, 0x21040, v5
	ds_read_b32 v5, v5
	v_and_b32_e32 v2, -16, v2
	v_ashrrev_i32_e32 v13, 6, v4
	s_ashr_i32 s8, s3, 2
	v_add_u32_e32 v146, v13, v2
	s_waitcnt lgkmcnt(0)
	v_sub_u32_e32 v2, s8, v5
	v_lshlrev_b32_e32 v7, 8, v2
	v_add_u32_e32 v2, v7, v1
	v_add_u32_e32 v4, v7, v146
	v_cmp_gt_i32_e32 vcc, 64, v3
	v_readfirstlane_b32 s6, v3
	v_add_u32_e32 v14, 0x80, v2
	v_add_u32_e32 v15, 0x80, v4
	s_cbranch_vccz .LBB0_1080
	s_lshl_b32 s2, s6, 13
	s_ashr_i32 s3, s2, 31
	s_lshl_b64 s[2:3], s[2:3], 2
	s_add_u32 s2, s31, s2
	s_addc_u32 s3, s33, s3
	v_ashrrev_i32_e32 v3, 31, v2
	v_lshl_add_u64 v[16:17], v[2:3], 2, s[2:3]
	v_ashrrev_i32_e32 v5, 31, v4
	v_lshl_add_u64 v[18:19], v[4:5], 2, s[2:3]
	global_load_dword v3, v[16:17], off
	global_load_dword v5, v[18:19], off
	global_load_dword v20, v[18:19], off offset:512
	global_load_dword v21, v[16:17], off offset:512
	s_lshl_b32 s2, s6, 2
	s_add_i32 s2, s2, 0
	s_add_i32 s2, s2, 0x21660
	v_mov_b32_e32 v16, s2
	s_waitcnt vmcnt(0)
	ds_read_b32 v17, v16
	v_lshlrev_b32_e32 v3, 12, v3
	v_lshlrev_b32_e32 v5, 12, v5
	v_lshlrev_b32_e32 v16, 12, v21
	v_lshlrev_b32_e32 v18, 12, v20
	s_waitcnt lgkmcnt(0)
	v_cmp_lt_i32_e32 vcc, v2, v17
	s_nop 1
	v_cndmask_b32_e32 v3, 0, v3, vcc
	v_cmp_lt_i32_e32 vcc, v4, v17
	s_nop 1
	v_cndmask_b32_e32 v5, 0, v5, vcc
	v_cmp_lt_i32_e32 vcc, v14, v17
	s_nop 1
	v_cndmask_b32_e32 v16, 0, v16, vcc
	v_cmp_lt_i32_e32 vcc, v15, v17
	s_nop 1
	v_cndmask_b32_e32 v17, 0, v18, vcc
	s_cbranch_execz .LBB0_1081
	s_branch .LBB0_1082

; #define PG8_STAGE(bufoff, gbase, v0, v1) do { \
;         __builtin_amdgcn_global_load_lds((const unsigned*)((const char*)(gbase) + (v0)), (LAS unsigned*)(lds + (bufoff) + ldsw), 16, 0, 0); \
;         __builtin_amdgcn_global_load_lds((const unsigned*)((const char*)(gbase) + (v1)), (LAS unsigned*)(lds + (bufoff) + ldsw + 8192), 16, 0, 0); } while (0)
; #define PG8_LDA(dst, b, h) do { _Pragma("unroll") for (int m = 0; m < 4; ++m) _Pragma("unroll") for (int k = 0; k < 2; ++k) dst[m][k] = *(const LAS bf16x8*)(lds + PG8_SA(b, h) + aoff + m * 2048 + k * 1024); } while (0)
; #define PG8_LDB(dst, b, h) do { _Pragma("unroll") for (int n = 0; n < 2; ++n) _Pragma("unroll") for (int k = 0; k < 2; ++k) dst[n][k] = *(const LAS bf16x8*)(lds + PG8_SB(b, h) + boff + n * 2048 + k * 1024); } while (0)
; #define PG8_MMA(ai, bj, At, Bt) do { __builtin_amdgcn_s_setprio(1); _Pragma("unroll") for (int m = 0; m < 4; ++m) _Pragma("unroll") for (int n = 0; n < 2; ++n) _Pragma("unroll") for (int k = 0; k < 2; ++k) \
;         acc[ai][bj][m][n] = __builtin_amdgcn_mfma_f32_16x16x32_bf16(Bt[n][k], At[m][k], acc[ai][bj][m][n], 0, 0, 0); __builtin_amdgcn_s_setprio(0); } while (0)
; #define PG8_WAIT_V(n) asm volatile("s_waitcnt vmcnt(" #n ")" ::: "memory")
; #define PG8_BAR __builtin_amdgcn_s_barrier()
; template <class Epi, class Sched>
; __device__ __forceinline__ void gemm_phase(LAS unsigned char* lds, const int K, const Sched& S, const Epi& E) {
;     ...
;             PG8_WAIT_V(6); PG8_BAR; PG8_MMA(1, 1, At, B1); PG8_BAR;
;             PG8_LDB(B0, 1, 0); PG8_SCHED; PG8_LDA(At, 1, 0); PG8_STAGE(PG8_SA(0, 1), a2, x10, x11);
; __device__ __forceinline__ bool bg_decode(int st, int wg, int NW, int lane, KP kp, const float*& src, int& ldS, bf16_t*& dst, int& o2) {
;     const int g = st * NW + wg;
;     if (g >= BG_STEPS) { src = kp->in[27] + lane; ldS = 0; dst = nullptr; o2 = 0; return false; }
;     const int l = g / 98304, r = g - l * 98304;
;     unsigned char* ws = kp->ws;
;     if (r < 65536) {
;         const int e = r >> 10, kc = (r >> 2) & 255, kind = (r >> 1) & 1, cc = r & 1, n = cc * 256 + lane;
;         ldS = FF; o2 = 256 * 8;
;         src = kp->in[27 + kind] + ((size_t)(l * NE + e) * D + kc * 8) * FF + n;
;         const int drow = (n >> 7) * 256 + kind * 128 + (n & 127);
;         dst = (bf16_t*)(ws + WS_WGU) + l * WGU_L + (size_t)e * 1024 * D + ((size_t)kc * 1024 + drow) * 8;
.Lpb8_p4j:
	s_barrier
	s_setprio 1
	v_mfma_f32_16x16x32_bf16 v[54:57], v[212:215], v[176:179], v[54:57]
	v_mfma_f32_16x16x32_bf16 v[50:53], v[220:223], v[176:179], v[50:53]
	v_mfma_f32_16x16x32_bf16 v[38:41], v[212:215], v[184:187], v[38:41]
	v_mfma_f32_16x16x32_bf16 v[34:37], v[220:223], v[184:187], v[34:37]
	v_mfma_f32_16x16x32_bf16 v[22:25], v[212:215], v[192:195], v[22:25]
	v_mfma_f32_16x16x32_bf16 v[18:21], v[220:223], v[192:195], v[18:21]
	v_mfma_f32_16x16x32_bf16 v[6:9], v[212:215], v[200:203], v[6:9]
	v_mfma_f32_16x16x32_bf16 v[2:5], v[220:223], v[200:203], v[2:5]
	v_mfma_f32_16x16x32_bf16 v[54:57], v[216:219], v[180:183], v[54:57]
	v_mfma_f32_16x16x32_bf16 v[50:53], v[224:227], v[180:183], v[50:53]
	v_mfma_f32_16x16x32_bf16 v[38:41], v[216:219], v[188:191], v[38:41]
	v_mfma_f32_16x16x32_bf16 v[34:37], v[224:227], v[188:191], v[34:37]
	v_mfma_f32_16x16x32_bf16 v[22:25], v[216:219], v[196:199], v[22:25]
	v_mfma_f32_16x16x32_bf16 v[18:21], v[224:227], v[196:199], v[18:21]
	v_mfma_f32_16x16x32_bf16 v[6:9], v[216:219], v[208:211], v[6:9]
	v_mfma_f32_16x16x32_bf16 v[2:5], v[224:227], v[208:211], v[2:5]
	s_setprio 0
	s_add_i32 s55, 0, 0x18000
	v_add_u32_e32 v134, s55, v149
	s_barrier
	ds_read_b128 v[160:163], v134
	ds_read_b128 v[164:167], v134 offset:1024
	ds_read_b128 v[168:171], v134 offset:2048
	ds_read_b128 v[172:175], v134 offset:3072
	s_mov_b32 m0, s39
	ds_read_b128 v[176:179], v151 offset:32768
	ds_read_b128 v[180:183], v151 offset:33792
	ds_read_b128 v[184:187], v151 offset:34816
	ds_read_b128 v[188:191], v151 offset:35840
	ds_read_b128 v[192:195], v151 offset:36864
	ds_read_b128 v[196:199], v151 offset:37888
	ds_read_b128 v[200:203], v151 offset:38912
	ds_read_b128 v[208:211], v151 offset:39936
	v_cndmask_b32_e32 v134, v140, v153, vcc
	global_load_lds_dwordx4 v139, s[26:27]
	s_mov_b32 m0, s40
	s_nop 0
	global_load_lds_dwordx4 v134, s[26:27]
	s_cmp_ge_u32 s70, 0x24000
	s_cbranch_scc1 .Lpb8_p5n
	s_cmp_eq_u32 s80, 0
	s_cbranch_scc0 .Lpb8_adv2
	s_cmp_ge_u32 s70, 0x18000
	s_cselect_b32 s84, 0x18000, 0
	s_cselect_b32 s83, 0x10000000, 0
	s_mov_b32 s81, 0x4030000
	s_cselect_b32 s81, 0x14430000, s81
	s_sub_u32 s84, s70, s84
	s_lshr_b32 s85, s84, 2
	s_lshl_b32 s85, s85, 14
	s_and_b32 s86, s84, 1
	s_lshl_b32 s87, s86, 10
	s_add_u32 s87, s87, s85
	s_add_u32 s87, s87, s83
	s_bitcmp1_b32 s84, 1
	s_cselect_b64 s[72:73], s[76:77], s[74:75]
	s_add_u32 s72, s72, s87
	s_addc_u32 s73, s73, 0
	s_add_u32 s88, s72, 0x2000
	s_addc_u32 s89, s73, 0
	s_lshl_b32 s86, s86, 13
	s_add_u32 s85, s85, s86
	s_and_b32 s86, s84, 2
	s_lshl_b32 s86, s86, 10
	s_add_u32 s85, s85, s86
	s_add_u32 s85, s85, s81
	v_add_u32_e32 v253, s85, v252
	s_movk_i32 s81, 0x400
	s_branch .Lpb8_ld2
